# router pass B: the trip's 4 x loads and 24 router-weight loads issued together at the top into their own registers (was 16 dependent round trips per trip); plus combine and diff-combine load batching
# speedup vs baseline: 1.0153x; 1.0066x over previous
; __device__ __forceinline__ unsigned pk2(float lo, float hi) { unsigned r; asm volatile("v_cvt_pk_bf16_f32 %0, %1, %2" : "=v"(r) : "v"(lo), "v"(hi)); return r; }
; #define LAS __attribute__((address_space(3)))
; __device__ __forceinline__ void ph_ln2_router(const P& p, int l, int row0, int G, int bid, int wave, int lane, LAS float* lds_f) {
;     ...
;     f32x4 acc[3] = {{0.f, 0.f, 0.f, 0.f}, {0.f, 0.f, 0.f, 0.f}, {0.f, 0.f, 0.f, 0.f}};
;     bf16_t* hn = WSP(bf16_t, WS_HN) + (size_t)row * DM + koff;
; #pragma unroll 4
;     for (int ks = 0; ks < 16; ++ks) { const int k = 32 * ks;
;       f32x4 x0, x1; ldx8(xr + k, x0, x1); const f32x4 g0 = *(const LAS f32x4*)(gs_ + k), g1 = *(const LAS f32x4*)(gs_ + k + 4);
;       const f32x4 sh0 = *(const LAS f32x4*)(sh_ + k), sh1 = *(const LAS f32x4*)(sh_ + k + 4);
;       float h[8];
; #pragma unroll
;       for (int j = 0; j < 4; ++j) { h[j] = x0[j] * rs * g0[j] + sh0[j]; h[4 + j] = x1[j] * rs * g1[j] + sh1[j]; }
;       u32x4 hw, lw;
; #pragma unroll
;       for (int j = 0; j < 4; ++j) { const unsigned hp = pk2(h[2 * j], h[2 * j + 1]); hw[j] = hp;
;         lw[j] = pk2(h[2 * j] - __uint_as_float(hp << 16), h[2 * j + 1] - __uint_as_float(hp & 0xffff0000u)); }
;       *(u32x4*)(hn + k) = hw;
;       const bf16x8 ah = __builtin_bit_cast(bf16x8, hw), al = __builtin_bit_cast(bf16x8, lw);
; #pragma unroll
;       for (int t = 0; t < 3; ++t) { const bf16x8 bh = *(const bf16x8*)(Wh + (size_t)(16 * t) * DM + k), bl = *(const bf16x8*)(Wl + (size_t)(16 * t) * DM + k);
;         acc[t] = __builtin_amdgcn_mfma_f32_16x16x32_bf16(ah, bh, acc[t], 0, 0, 0);
;         acc[t] = __builtin_amdgcn_mfma_f32_16x16x32_bf16(al, bh, acc[t], 0, 0, 0);
;         acc[t] = __builtin_amdgcn_mfma_f32_16x16x32_bf16(ah, bl, acc[t], 0, 0, 0); }
;     }
.LBB0_788:
	v_lshl_add_u64 v[40:41], v[30:31], 0, s[38:39]
	v_add_co_u32_e32 v44, vcc, s6, v40
	s_mov_b32 s3, 0x37dee000
	s_nop 0
	v_addc_co_u32_e32 v45, vcc, 0, v41, vcc
	global_load_dwordx4 v[12:15], v[44:45], off
	v_lshl_add_u64 v[70:71], v[24:25], 0, s[38:39]
	s_mov_b64 s[40:41], 0x37dee000
	v_lshl_add_u64 v[72:73], v[70:71], 0, s[40:41]
	s_mov_b64 s[40:41], 0x37e1e000
	v_lshl_add_u64 v[74:75], v[70:71], 0, s[40:41]
	s_mov_b64 s[40:41], 0x37dfe000
	v_lshl_add_u64 v[76:77], v[70:71], 0, s[40:41]
	s_mov_b64 s[40:41], 0x37e2e000
	v_lshl_add_u64 v[78:79], v[70:71], 0, s[40:41]
	s_mov_b64 s[40:41], 0x37e0e000
	v_lshl_add_u64 v[80:81], v[70:71], 0, s[40:41]
	s_mov_b64 s[40:41], 0x37e3e000
	v_lshl_add_u64 v[82:83], v[70:71], 0, s[40:41]
	global_load_dwordx4 v[84:87], v[72:73], off
	global_load_dwordx4 v[88:91], v[74:75], off
	global_load_dwordx4 v[92:95], v[76:77], off
	global_load_dwordx4 v[100:103], v[78:79], off
	global_load_dwordx4 v[104:107], v[80:81], off
	global_load_dwordx4 v[108:111], v[82:83], off
	global_load_dwordx4 v[112:115], v[44:45], off offset:64
	global_load_dwordx4 v[116:119], v[72:73], off offset:64
	global_load_dwordx4 v[120:123], v[74:75], off offset:64
	global_load_dwordx4 v[124:127], v[76:77], off offset:64
	global_load_dwordx4 v[128:131], v[78:79], off offset:64
	global_load_dwordx4 v[132:135], v[80:81], off offset:64
	global_load_dwordx4 v[136:139], v[82:83], off offset:64
	global_load_dwordx4 v[140:143], v[44:45], off offset:128
	global_load_dwordx4 v[144:147], v[72:73], off offset:128
	global_load_dwordx4 v[152:155], v[74:75], off offset:128
	global_load_dwordx4 v[156:159], v[76:77], off offset:128
	global_load_dwordx4 v[160:163], v[78:79], off offset:128
	global_load_dwordx4 v[164:167], v[80:81], off offset:128
	global_load_dwordx4 v[168:171], v[82:83], off offset:128
	global_load_dwordx4 v[172:175], v[44:45], off offset:192
	global_load_dwordx4 v[180:183], v[72:73], off offset:192
	global_load_dwordx4 v[184:187], v[74:75], off offset:192
	global_load_dwordx4 v[188:191], v[76:77], off offset:192
	global_load_dwordx4 v[192:195], v[78:79], off offset:192
	global_load_dwordx4 v[196:199], v[80:81], off offset:192
	global_load_dwordx4 v[200:203], v[82:83], off offset:192
	s_waitcnt vmcnt(0)
	v_lshlrev_b32_e32 v42, 16, v12
	v_and_b32_e32 v43, 0xffff0000, v12
	v_lshlrev_b32_e32 v46, 16, v13
	v_and_b32_e32 v47, 0xffff0000, v13
	v_lshlrev_b32_e32 v54, 16, v14
	v_and_b32_e32 v55, 0xffff0000, v14
	v_lshlrev_b32_e32 v56, 16, v15
	v_and_b32_e32 v57, 0xffff0000, v15
	ds_read_b128 v[12:15], v53
	ds_read_b128 v[16:19], v53 offset:16
	ds_read_b128 v[32:35], v53 offset:16384
	ds_read_b128 v[36:39], v53 offset:16400
	v_mul_f32_e32 v42, v29, v42
	s_waitcnt lgkmcnt(1)
	v_fma_f32 v32, v12, v42, v32
	v_mul_f32_e32 v12, v29, v54
	s_waitcnt lgkmcnt(0)
	v_fma_f32 v36, v16, v12, v36
	v_mul_f32_e32 v12, v29, v43
	v_fma_f32 v13, v13, v12, v33
	v_mul_f32_e32 v12, v29, v55
	v_fma_f32 v33, v17, v12, v37
	v_mul_f32_e32 v12, v29, v46
	v_fma_f32 v14, v14, v12, v34
	v_mul_f32_e32 v12, v29, v56
	v_fma_f32 v34, v18, v12, v38
	v_mul_f32_e32 v12, v29, v47
	v_fmac_f32_e32 v35, v15, v12
	v_mul_f32_e32 v12, v29, v57
	v_fmac_f32_e32 v39, v19, v12
	v_cvt_pk_bf16_f32 v12, v32, v13
	v_lshl_add_u64 v[46:47], v[24:25], 0, s[38:39]
	v_lshlrev_b32_e32 v15, 16, v12
	v_and_b32_e32 v16, 0xffff0000, v12
	v_sub_f32_e32 v15, v32, v15
	v_sub_f32_e32 v13, v13, v16
	v_cvt_pk_bf16_f32 v16, v15, v13
	v_cvt_pk_bf16_f32 v13, v14, v35
	s_add_u32 s38, s38, 0x100
	v_lshlrev_b32_e32 v15, 16, v13
	v_sub_f32_e32 v14, v14, v15
	v_and_b32_e32 v15, 0xffff0000, v13
	v_sub_f32_e32 v15, v35, v15
	v_cvt_pk_bf16_f32 v17, v14, v15
	v_cvt_pk_bf16_f32 v14, v36, v33
	s_addc_u32 s39, s39, 0
	v_lshlrev_b32_e32 v15, 16, v14
	v_and_b32_e32 v18, 0xffff0000, v14
	v_sub_f32_e32 v15, v36, v15
	v_sub_f32_e32 v18, v33, v18
	v_cvt_pk_bf16_f32 v18, v15, v18
	v_cvt_pk_bf16_f32 v15, v34, v39
	s_cmpk_eq_i32 s38, 0x400
	v_lshlrev_b32_e32 v19, 16, v15
	v_and_b32_e32 v32, 0xffff0000, v15
	v_sub_f32_e32 v19, v34, v19
	v_sub_f32_e32 v32, v39, v32
	v_cvt_pk_bf16_f32 v19, v19, v32
	v_add_co_u32_e32 v32, vcc, s7, v40
	s_nop 1
	v_addc_co_u32_e32 v33, vcc, 0, v41, vcc
	v_add_co_u32_e32 v34, vcc, s3, v46
	global_store_dwordx4 v[32:33], v[12:15], off
	s_nop 1
	s_nop 0
	v_addc_co_u32_e32 v35, vcc, 0, v47, vcc
	s_mov_b32 s3, 0x37e1e000
	v_add_co_u32_e32 v36, vcc, s3, v46
	s_mov_b32 s3, 0x37dfe000
	s_nop 0
	v_addc_co_u32_e32 v37, vcc, 0, v47, vcc
	v_mfma_f32_16x16x32_bf16 v[4:7], v[12:15], v[84:87], v[4:7]
	v_mfma_f32_16x16x32_bf16 v[4:7], v[16:19], v[84:87], v[4:7]
	v_add_co_u32_e32 v38, vcc, s3, v46
	s_mov_b32 s3, 0x37e2e000
	s_nop 0
	v_addc_co_u32_e32 v39, vcc, 0, v47, vcc
	v_mfma_f32_16x16x32_bf16 v[4:7], v[12:15], v[88:91], v[4:7]
	v_add_co_u32_e32 v40, vcc, s3, v46
	s_mov_b32 s3, 0x37e0e000
	s_nop 0
	v_addc_co_u32_e32 v41, vcc, 0, v47, vcc
	v_add_co_u32_e32 v42, vcc, s3, v46
	s_mov_b32 s3, 0x37e3e000
	s_nop 0
	v_addc_co_u32_e32 v43, vcc, 0, v47, vcc
	v_add_co_u32_e32 v46, vcc, s3, v46
	v_mfma_f32_16x16x32_bf16 v[8:11], v[12:15], v[92:95], v[8:11]
	v_addc_co_u32_e32 v47, vcc, 0, v47, vcc
	v_mfma_f32_16x16x32_bf16 v[8:11], v[16:19], v[92:95], v[8:11]
	v_mfma_f32_16x16x32_bf16 v[8:11], v[12:15], v[100:103], v[8:11]
	v_mfma_f32_16x16x32_bf16 v[0:3], v[12:15], v[104:107], v[0:3]
	v_mfma_f32_16x16x32_bf16 v[0:3], v[16:19], v[104:107], v[0:3]
	v_mfma_f32_16x16x32_bf16 v[0:3], v[12:15], v[108:111], v[0:3]
	v_lshlrev_b32_e32 v62, 16, v112
	v_and_b32_e32 v63, 0xffff0000, v112
	v_lshlrev_b32_e32 v64, 16, v113
	v_and_b32_e32 v65, 0xffff0000, v113
	v_lshlrev_b32_e32 v66, 16, v114
	v_and_b32_e32 v67, 0xffff0000, v114
	v_lshlrev_b32_e32 v68, 16, v115
	v_and_b32_e32 v69, 0xffff0000, v115
	ds_read_b128 v[12:15], v53 offset:128
	ds_read_b128 v[16:19], v53 offset:144
	ds_read_b128 v[54:57], v53 offset:16512
	ds_read_b128 v[58:61], v53 offset:16528
	v_mul_f32_e32 v62, v29, v62
	s_waitcnt lgkmcnt(1)
; __device__ __forceinline__ unsigned pk2(float lo, float hi) { unsigned r; asm volatile("v_cvt_pk_bf16_f32 %0, %1, %2" : "=v"(r) : "v"(lo), "v"(hi)); return r; }
; #define LAS __attribute__((address_space(3)))
; __device__ __forceinline__ void ph_ln2_router(const P& p, int l, int row0, int G, int bid, int wave, int lane, LAS float* lds_f) {
;     ...
; #pragma unroll 4
;     for (int ks = 0; ks < 16; ++ks) { const int k = 32 * ks;
;       f32x4 x0, x1; ldx8(xr + k, x0, x1); const f32x4 g0 = *(const LAS f32x4*)(gs_ + k), g1 = *(const LAS f32x4*)(gs_ + k + 4);
;       const f32x4 sh0 = *(const LAS f32x4*)(sh_ + k), sh1 = *(const LAS f32x4*)(sh_ + k + 4);
;       float h[8];
; #pragma unroll
;       for (int j = 0; j < 4; ++j) { h[j] = x0[j] * rs * g0[j] + sh0[j]; h[4 + j] = x1[j] * rs * g1[j] + sh1[j]; }
;       u32x4 hw, lw;
; #pragma unroll
;       for (int j = 0; j < 4; ++j) { const unsigned hp = pk2(h[2 * j], h[2 * j + 1]); hw[j] = hp;
;         lw[j] = pk2(h[2 * j] - __uint_as_float(hp << 16), h[2 * j + 1] - __uint_as_float(hp & 0xffff0000u)); }
;       *(u32x4*)(hn + k) = hw;
;       const bf16x8 ah = __builtin_bit_cast(bf16x8, hw), al = __builtin_bit_cast(bf16x8, lw);
; #pragma unroll
;       for (int t = 0; t < 3; ++t) { const bf16x8 bh = *(const bf16x8*)(Wh + (size_t)(16 * t) * DM + k), bl = *(const bf16x8*)(Wl + (size_t)(16 * t) * DM + k);
;         acc[t] = __builtin_amdgcn_mfma_f32_16x16x32_bf16(ah, bh, acc[t], 0, 0, 0);
;         acc[t] = __builtin_amdgcn_mfma_f32_16x16x32_bf16(al, bh, acc[t], 0, 0, 0);
;         acc[t] = __builtin_amdgcn_mfma_f32_16x16x32_bf16(ah, bl, acc[t], 0, 0, 0); }
;     }
	v_fma_f32 v54, v12, v62, v54
	v_mul_f32_e32 v12, v29, v66
	s_waitcnt lgkmcnt(0)
	v_fma_f32 v58, v16, v12, v58
	v_mul_f32_e32 v12, v29, v63
	v_fma_f32 v13, v13, v12, v55
	v_mul_f32_e32 v12, v29, v67
	v_fma_f32 v55, v17, v12, v59
	v_mul_f32_e32 v12, v29, v64
	v_fma_f32 v14, v14, v12, v56
	v_mul_f32_e32 v12, v29, v68
	v_fma_f32 v56, v18, v12, v60
	v_mul_f32_e32 v12, v29, v65
	v_fmac_f32_e32 v57, v15, v12
	v_mul_f32_e32 v12, v29, v69
	v_fmac_f32_e32 v61, v19, v12
	v_cvt_pk_bf16_f32 v12, v54, v13
	s_nop 0
	v_lshlrev_b32_e32 v15, 16, v12
	v_and_b32_e32 v16, 0xffff0000, v12
	v_sub_f32_e32 v15, v54, v15
	v_sub_f32_e32 v13, v13, v16
	v_cvt_pk_bf16_f32 v16, v15, v13
	v_cvt_pk_bf16_f32 v13, v14, v57
	s_nop 0
	v_lshlrev_b32_e32 v15, 16, v13
	v_sub_f32_e32 v14, v14, v15
	v_and_b32_e32 v15, 0xffff0000, v13
	v_sub_f32_e32 v15, v57, v15
	v_cvt_pk_bf16_f32 v17, v14, v15
	v_cvt_pk_bf16_f32 v14, v58, v55
	s_nop 0
	v_lshlrev_b32_e32 v15, 16, v14
	v_and_b32_e32 v18, 0xffff0000, v14
	v_sub_f32_e32 v15, v58, v15
	v_sub_f32_e32 v18, v55, v18
	v_cvt_pk_bf16_f32 v18, v15, v18
	v_cvt_pk_bf16_f32 v15, v56, v61
	s_nop 0
	v_lshlrev_b32_e32 v19, 16, v15
	v_sub_f32_e32 v19, v56, v19
	v_and_b32_e32 v54, 0xffff0000, v15
	v_sub_f32_e32 v54, v61, v54
	v_cvt_pk_bf16_f32 v19, v19, v54
	global_store_dwordx4 v[32:33], v[12:15], off offset:64
	s_nop 1
	v_mfma_f32_16x16x32_bf16 v[4:7], v[12:15], v[116:119], v[4:7]
	v_mfma_f32_16x16x32_bf16 v[4:7], v[16:19], v[116:119], v[4:7]
	v_mfma_f32_16x16x32_bf16 v[4:7], v[12:15], v[120:123], v[4:7]
	v_mfma_f32_16x16x32_bf16 v[8:11], v[12:15], v[124:127], v[8:11]
	v_mfma_f32_16x16x32_bf16 v[8:11], v[16:19], v[124:127], v[8:11]
	v_mfma_f32_16x16x32_bf16 v[8:11], v[12:15], v[128:131], v[8:11]
	v_mfma_f32_16x16x32_bf16 v[0:3], v[12:15], v[132:135], v[0:3]
	v_mfma_f32_16x16x32_bf16 v[0:3], v[16:19], v[132:135], v[0:3]
	v_mfma_f32_16x16x32_bf16 v[0:3], v[12:15], v[136:139], v[0:3]
	v_lshlrev_b32_e32 v62, 16, v140
	v_and_b32_e32 v63, 0xffff0000, v140
	v_lshlrev_b32_e32 v64, 16, v141
	v_and_b32_e32 v65, 0xffff0000, v141
	v_lshlrev_b32_e32 v66, 16, v142
	v_and_b32_e32 v67, 0xffff0000, v142
	v_lshlrev_b32_e32 v68, 16, v143
	v_and_b32_e32 v69, 0xffff0000, v143
	ds_read_b128 v[12:15], v53 offset:256
	ds_read_b128 v[16:19], v53 offset:272
	ds_read_b128 v[54:57], v53 offset:16640
	ds_read_b128 v[58:61], v53 offset:16656
	v_mul_f32_e32 v62, v29, v62
	s_waitcnt lgkmcnt(1)
	v_fma_f32 v54, v12, v62, v54
	v_mul_f32_e32 v12, v29, v66
	s_waitcnt lgkmcnt(0)
	v_fma_f32 v58, v16, v12, v58
	v_mul_f32_e32 v12, v29, v63
	v_fma_f32 v13, v13, v12, v55
	v_mul_f32_e32 v12, v29, v67
	v_fma_f32 v55, v17, v12, v59
	v_mul_f32_e32 v12, v29, v64
	v_fma_f32 v14, v14, v12, v56
	v_mul_f32_e32 v12, v29, v68
	v_fma_f32 v56, v18, v12, v60
	v_mul_f32_e32 v12, v29, v65
	v_fmac_f32_e32 v57, v15, v12
	v_mul_f32_e32 v12, v29, v69
	v_fmac_f32_e32 v61, v19, v12
	v_cvt_pk_bf16_f32 v12, v54, v13
	s_nop 0
	v_lshlrev_b32_e32 v15, 16, v12
	v_and_b32_e32 v16, 0xffff0000, v12
	v_sub_f32_e32 v15, v54, v15
	v_sub_f32_e32 v13, v13, v16
	v_cvt_pk_bf16_f32 v16, v15, v13
	v_cvt_pk_bf16_f32 v13, v14, v57
	s_nop 0
	v_lshlrev_b32_e32 v15, 16, v13
	v_sub_f32_e32 v14, v14, v15
	v_and_b32_e32 v15, 0xffff0000, v13
	v_sub_f32_e32 v15, v57, v15
	v_cvt_pk_bf16_f32 v17, v14, v15
	v_cvt_pk_bf16_f32 v14, v58, v55
	s_nop 0
	v_lshlrev_b32_e32 v15, 16, v14
	v_and_b32_e32 v18, 0xffff0000, v14
	v_sub_f32_e32 v15, v58, v15
	v_sub_f32_e32 v18, v55, v18
	v_cvt_pk_bf16_f32 v18, v15, v18
	v_cvt_pk_bf16_f32 v15, v56, v61
	s_nop 0
	v_lshlrev_b32_e32 v19, 16, v15
	v_sub_f32_e32 v19, v56, v19
	v_and_b32_e32 v54, 0xffff0000, v15
	v_sub_f32_e32 v54, v61, v54
	v_cvt_pk_bf16_f32 v19, v19, v54
	global_store_dwordx4 v[32:33], v[12:15], off offset:128
	s_nop 1
	v_mfma_f32_16x16x32_bf16 v[4:7], v[12:15], v[144:147], v[4:7]
	v_mfma_f32_16x16x32_bf16 v[4:7], v[16:19], v[144:147], v[4:7]
	v_mfma_f32_16x16x32_bf16 v[4:7], v[12:15], v[152:155], v[4:7]
	v_mfma_f32_16x16x32_bf16 v[8:11], v[12:15], v[156:159], v[8:11]
	v_mfma_f32_16x16x32_bf16 v[8:11], v[16:19], v[156:159], v[8:11]
	v_mfma_f32_16x16x32_bf16 v[8:11], v[12:15], v[160:163], v[8:11]
	v_mfma_f32_16x16x32_bf16 v[0:3], v[12:15], v[164:167], v[0:3]
	v_mfma_f32_16x16x32_bf16 v[0:3], v[16:19], v[164:167], v[0:3]
	v_mfma_f32_16x16x32_bf16 v[0:3], v[12:15], v[168:171], v[0:3]
	v_lshlrev_b32_e32 v44, 16, v172
	v_and_b32_e32 v45, 0xffff0000, v172
	v_lshlrev_b32_e32 v62, 16, v173
	v_and_b32_e32 v63, 0xffff0000, v173
	v_lshlrev_b32_e32 v64, 16, v174
	v_and_b32_e32 v65, 0xffff0000, v174
	v_lshlrev_b32_e32 v66, 16, v175
	v_and_b32_e32 v67, 0xffff0000, v175
	ds_read_b128 v[12:15], v53 offset:384
	ds_read_b128 v[16:19], v53 offset:400
	ds_read_b128 v[54:57], v53 offset:16768
	ds_read_b128 v[58:61], v53 offset:16784
	v_mul_f32_e32 v44, v29, v44
	v_add_u32_e32 v53, 0x200, v53
	s_waitcnt lgkmcnt(1)
	v_fma_f32 v44, v12, v44, v54
	v_mul_f32_e32 v12, v29, v64
	s_waitcnt lgkmcnt(0)
	v_fma_f32 v54, v16, v12, v58
	v_mul_f32_e32 v12, v29, v45
	v_fma_f32 v13, v13, v12, v55
	v_mul_f32_e32 v12, v29, v65
	v_fma_f32 v45, v17, v12, v59
	v_mul_f32_e32 v12, v29, v62
	v_fma_f32 v14, v14, v12, v56
	v_mul_f32_e32 v12, v29, v66
	v_fma_f32 v55, v18, v12, v60
	v_mul_f32_e32 v12, v29, v63
	v_fmac_f32_e32 v57, v15, v12
	v_mul_f32_e32 v12, v29, v67
	v_fmac_f32_e32 v61, v19, v12
	v_cvt_pk_bf16_f32 v12, v44, v13
	s_nop 0
	v_lshlrev_b32_e32 v15, 16, v12
	v_and_b32_e32 v16, 0xffff0000, v12
	v_sub_f32_e32 v15, v44, v15
	v_sub_f32_e32 v13, v13, v16
	v_cvt_pk_bf16_f32 v16, v15, v13
	v_cvt_pk_bf16_f32 v13, v14, v57
	s_nop 0
	v_lshlrev_b32_e32 v15, 16, v13
	v_sub_f32_e32 v14, v14, v15
	v_and_b32_e32 v15, 0xffff0000, v13
	v_sub_f32_e32 v15, v57, v15
	v_cvt_pk_bf16_f32 v17, v14, v15
	v_cvt_pk_bf16_f32 v14, v54, v45
	s_nop 0
	v_lshlrev_b32_e32 v15, 16, v14
	v_and_b32_e32 v18, 0xffff0000, v14
	v_sub_f32_e32 v15, v54, v15
	v_sub_f32_e32 v18, v45, v18
	v_cvt_pk_bf16_f32 v18, v15, v18
	v_cvt_pk_bf16_f32 v15, v55, v61
	s_nop 0
	v_lshlrev_b32_e32 v19, 16, v15
	v_sub_f32_e32 v19, v55, v19
	v_and_b32_e32 v44, 0xffff0000, v15
	v_sub_f32_e32 v44, v61, v44
	v_cvt_pk_bf16_f32 v19, v19, v44
	global_store_dwordx4 v[32:33], v[12:15], off offset:192
	s_nop 1
	s_nop 0
	v_mfma_f32_16x16x32_bf16 v[4:7], v[12:15], v[180:183], v[4:7]
	v_mfma_f32_16x16x32_bf16 v[4:7], v[16:19], v[180:183], v[4:7]
	s_nop 0
	v_mfma_f32_16x16x32_bf16 v[8:11], v[12:15], v[188:191], v[8:11]
	v_mfma_f32_16x16x32_bf16 v[8:11], v[16:19], v[188:191], v[8:11]
	v_mfma_f32_16x16x32_bf16 v[8:11], v[12:15], v[192:195], v[8:11]
	v_mfma_f32_16x16x32_bf16 v[0:3], v[12:15], v[196:199], v[0:3]
	v_mfma_f32_16x16x32_bf16 v[0:3], v[16:19], v[196:199], v[0:3]
	v_mfma_f32_16x16x32_bf16 v[4:7], v[12:15], v[184:187], v[4:7]
	v_mfma_f32_16x16x32_bf16 v[0:3], v[12:15], v[200:203], v[0:3]
	s_cbranch_scc0 .LBB0_788
; #define LAS __attribute__((address_space(3)))
; template <class F> __device__ __forceinline__ int2 route_pick(const P& p, int l, int r, F lg) {
;   float gl[4];
; #pragma unroll
;   for (int u = 0; u < 4; ++u) gl[u] = lg(u) + p.rgb[l * NGRP + u];
;   int gi = 0; float gm = gl[0];
; #pragma unroll
;   for (int u = 1; u < 4; ++u) if (gl[u] > gm) { gm = gl[u]; gi = u; }
;   float gs = 0.f;
; #pragma unroll
;   for (int u = 0; u < 4; ++u) gs += expf(gl[u] - gm);
;   const float gtop = 1.f / gs;
;   float es[8];
; #pragma unroll
;   for (int u = 0; u < 8; ++u) es[u] = lg(4 + gi * 8 + u) + p.reb[l * NEXP + gi * 8 + u];
;   int i0 = 0; float m0 = es[0];
; #pragma unroll
;   for (int u = 1; u < 8; ++u) if (es[u] > m0) { m0 = es[u]; i0 = u; }
; __device__ __forceinline__ void ph_ln2_router(const P& p, int l, int row0, int G, int bid, int wave, int lane, LAS float* lds_f) {
;     ...
; #pragma unroll
;     for (int t = 0; t < 3; ++t)
; #pragma unroll
;       for (int rg = 0; rg < 4; ++rg) part[(wave * 16 + 4 * q + rg) * 49 + 16 * t + r16] = acc[t][rg];
;     __syncthreads();
;     if (kq == 0 && lane < 16) {
;       const LAS float* l0 = part + ((grp * 4 + 0) * 16 + lane) * 49; const LAS float* l1 = l0 + 16 * 49; const LAS float* l2 = l1 + 16 * 49; const LAS float* l3 = l2 + 16 * 49;
;       const int2 ee = route_pick(p, l, rbase + lane, [&](int n) { return (l0[n] + l1[n]) + (l2[n] + l3[n]); });
	s_nop 4
	ds_write2_b32 v52, v4, v8 offset0:128 offset1:144
	ds_write2_b32 v52, v6, v10 offset0:226 offset1:242
	ds_write2_b32 v52, v0, v5 offset0:160 offset1:177
	ds_write2_b32 v52, v9, v1 offset0:193 offset1:209
	v_add_u32_e32 v0, 0x400, v52
	ds_write2_b32 v0, v2, v7 offset0:2 offset1:19
	ds_write2_b32 v0, v11, v3 offset0:35 offset1:51
	s_waitcnt lgkmcnt(0)
	s_barrier
	s_and_saveexec_b64 s[38:39], s[20:21]
	s_cbranch_execz .LBB0_795
	v_add_u32_e32 v2, 0xe40, v49
	v_add_u32_e32 v4, 0x1a80, v49
	v_add_u32_e32 v6, 0x26c0, v49
	ds_read2_b32 v[0:1], v49 offset0:128 offset1:129
	ds_read2_b32 v[2:3], v2 offset1:1
	ds_read2_b32 v[4:5], v4 offset1:1
	ds_read2_b32 v[6:7], v6 offset1:1
	s_mov_b32 s3, 0xff800000
	s_waitcnt lgkmcnt(3)
	v_mov_b32_e32 v8, v0
	s_waitcnt lgkmcnt(2)
	v_mov_b32_e32 v10, v2
	s_waitcnt lgkmcnt(1)
	v_mov_b32_e32 v9, v4
	s_waitcnt lgkmcnt(0)
	v_mov_b32_e32 v11, v6
	v_mov_b32_e32 v4, v1
	v_mov_b32_e32 v6, v3
	v_pk_add_f32 v[8:9], v[8:9], v[10:11]
	v_pk_add_f32 v[0:1], v[4:5], v[6:7]
	v_mov_b32_e32 v2, v8
	v_mov_b32_e32 v3, v0
	v_mov_b32_e32 v0, v9
	v_pk_add_f32 v[4:5], v[2:3], v[0:1]
	global_load_dwordx4 v[0:3], v97, s[22:23]
	v_add_u32_e32 v6, 0xe48, v49
	v_add_u32_e32 v8, 0x1a88, v49
	ds_read2_b32 v[6:7], v6 offset1:1
	ds_read2_b32 v[10:11], v8 offset1:1
	v_add_u32_e32 v8, 0x26c8, v49
	ds_read2_b32 v[12:13], v8 offset1:1
	s_waitcnt lgkmcnt(2)
	v_mov_b32_e32 v14, v6
	s_waitcnt lgkmcnt(1)
	v_mov_b32_e32 v9, v10
	s_waitcnt lgkmcnt(0)
	v_mov_b32_e32 v15, v12
	v_mov_b32_e32 v12, v7
	s_waitcnt vmcnt(0)
	v_pk_add_f32 v[4:5], v[0:1], v[4:5]
	ds_read2_b32 v[0:1], v49 offset0:130 offset1:131
	v_cmp_gt_f32_e64 s[40:41], v5, v4
	s_waitcnt lgkmcnt(0)
	v_mov_b32_e32 v8, v0
	v_pk_add_f32 v[8:9], v[8:9], v[14:15]
	v_mov_b32_e32 v10, v1
	v_add_f32_e32 v0, v8, v9
	v_add_f32_e32 v9, v2, v0
	v_pk_add_f32 v[0:1], v[10:11], v[12:13]
	s_nop 0
	v_add_f32_e32 v0, v0, v1
	v_add_f32_e32 v10, v3, v0
	v_cndmask_b32_e64 v0, v4, v5, s[40:41]
	v_cmp_gt_f32_e64 s[42:43], v9, v0
	s_nop 1
	v_cndmask_b32_e64 v11, v0, v9, s[42:43]
	v_cndmask_b32_e64 v0, 0, 8, s[40:41]
	v_cmp_gt_f32_e32 vcc, v10, v11
	v_cndmask_b32_e64 v0, v0, 16, s[42:43]
	s_nop 0
	v_cndmask_b32_e64 v8, v0, 24, vcc
	v_lshl_add_u32 v29, v8, 2, v49
	v_add_u32_e32 v1, 0xe50, v29
	ds_read2_b32 v[2:3], v29 offset0:132 offset1:133
	ds_read2_b32 v[6:7], v1 offset1:1
	v_add_u32_e32 v1, 0x1a90, v29
	ds_read2_b32 v[12:13], v1 offset1:1
	v_add_u32_e32 v1, 0x26d0, v29
	ds_read2_b32 v[14:15], v1 offset1:1
	v_or_b32_e32 v0, s4, v8
	s_waitcnt lgkmcnt(3)
	v_mov_b32_e32 v16, v2
	s_waitcnt lgkmcnt(1)
	v_mov_b32_e32 v17, v12
	v_mov_b32_e32 v18, v6
	s_waitcnt lgkmcnt(0)
	v_mov_b32_e32 v19, v14
	v_ashrrev_i32_e32 v1, 31, v0
	v_mov_b32_e32 v12, v3
	v_mov_b32_e32 v14, v7
	v_pk_add_f32 v[16:17], v[16:17], v[18:19]
	v_lshl_add_u64 v[18:19], v[0:1], 2, s[58:59]
	v_pk_add_f32 v[0:1], v[12:13], v[14:15]
	v_mov_b32_e32 v2, v16
	v_mov_b32_e32 v3, v0
	v_mov_b32_e32 v0, v17
	v_pk_add_f32 v[6:7], v[2:3], v[0:1]
	global_load_dwordx4 v[0:3], v[18:19], off offset:16
	global_load_dwordx4 v[12:15], v[18:19], off
	ds_read2_b32 v[16:17], v29 offset0:134 offset1:135
	s_waitcnt vmcnt(0)
	v_pk_add_f32 v[6:7], v[12:13], v[6:7]
	v_add_u32_e32 v12, 0xe58, v29
	ds_read2_b32 v[18:19], v12 offset1:1
	v_add_u32_e32 v12, 0x1a98, v29
	ds_read2_b32 v[30:31], v12 offset1:1
	v_add_u32_e32 v12, 0x26d8, v29
	ds_read2_b32 v[32:33], v12 offset1:1
	s_waitcnt lgkmcnt(3)
	v_mov_b32_e32 v12, v16
	s_waitcnt lgkmcnt(2)
	v_mov_b32_e32 v34, v18
	s_waitcnt lgkmcnt(1)
	v_mov_b32_e32 v13, v30
	v_mov_b32_e32 v30, v17
	s_waitcnt lgkmcnt(0)
; template <class F> __device__ __forceinline__ int2 route_pick(const P& p, int l, int r, F lg) {
;     ...
;   for (int u = 0; u < 8; ++u) es[u] = lg(4 + gi * 8 + u) + p.reb[l * NEXP + gi * 8 + u];
;   int i0 = 0; float m0 = es[0];
; #pragma unroll
;   for (int u = 1; u < 8; ++u) if (es[u] > m0) { m0 = es[u]; i0 = u; }
;   int i1 = -1; float m1 = -INFINITY;
; #pragma unroll
;   for (int u = 0; u < 8; ++u) if (u != i0 && es[u] > m1) { m1 = es[u]; i1 = u; }
	v_mov_b32_e32 v35, v32
	v_pk_add_f32 v[12:13], v[12:13], v[34:35]
	v_mov_b32_e32 v32, v19
	v_add_f32_e32 v12, v12, v13
	v_add_f32_e32 v13, v14, v12
	v_pk_add_f32 v[16:17], v[30:31], v[32:33]
	v_add_u32_e32 v14, 0xe60, v29
	v_add_f32_e32 v12, v16, v17
	ds_read2_b32 v[16:17], v29 offset0:136 offset1:137
	ds_read2_b32 v[18:19], v14 offset1:1
	v_add_u32_e32 v14, 0x1aa0, v29
	ds_read2_b32 v[30:31], v14 offset1:1
	v_add_u32_e32 v14, 0x26e0, v29
	ds_read2_b32 v[32:33], v14 offset1:1
	v_add_f32_e32 v12, v15, v12
	s_waitcnt lgkmcnt(3)
	v_mov_b32_e32 v14, v16
	s_waitcnt lgkmcnt(1)
	v_mov_b32_e32 v15, v30
	v_mov_b32_e32 v34, v18
	s_waitcnt lgkmcnt(0)
	v_mov_b32_e32 v35, v32
	v_pk_add_f32 v[14:15], v[14:15], v[34:35]
	v_mov_b32_e32 v30, v17
	v_mov_b32_e32 v32, v19
	v_add_f32_e32 v14, v14, v15
	v_pk_add_f32 v[16:17], v[30:31], v[32:33]
	v_add_f32_e32 v15, v0, v14
	v_add_f32_e32 v0, v16, v17
	v_add_f32_e32 v14, v1, v0
	ds_read2_b32 v[0:1], v29 offset0:138 offset1:139
	v_add_u32_e32 v16, 0xe68, v29
	v_add_u32_e32 v18, 0x1aa8, v29
	v_add_u32_e32 v29, 0x26e8, v29
	ds_read2_b32 v[16:17], v16 offset1:1
	ds_read2_b32 v[18:19], v18 offset1:1
	ds_read2_b32 v[30:31], v29 offset1:1
	s_waitcnt lgkmcnt(3)
	v_mov_b32_e32 v32, v0
	v_cmp_gt_f32_e64 s[40:41], v7, v6
	s_waitcnt lgkmcnt(2)
	v_mov_b32_e32 v34, v16
	s_waitcnt lgkmcnt(1)
	v_mov_b32_e32 v33, v18
	s_waitcnt lgkmcnt(0)
	v_mov_b32_e32 v35, v30
	v_pk_add_f32 v[32:33], v[32:33], v[34:35]
	v_mov_b32_e32 v18, v1
	v_add_f32_e32 v0, v32, v33
	v_mov_b32_e32 v30, v17
	v_add_f32_e32 v2, v2, v0
	v_pk_add_f32 v[0:1], v[18:19], v[30:31]
	v_cmp_nlg_f32_e64 s[48:49], s3, v6
	v_add_f32_e32 v0, v0, v1
	v_add_f32_e32 v1, v3, v0
	v_cndmask_b32_e64 v3, v6, v7, s[40:41]
	v_cndmask_b32_e64 v0, 0, 1, s[40:41]
	v_cmp_gt_f32_e64 s[40:41], v13, v3
	v_mov_b32_e32 v17, 0xff800000
	s_nop 0
	v_cndmask_b32_e64 v3, v3, v13, s[40:41]
	v_cndmask_b32_e64 v0, v0, 2, s[40:41]
	v_cmp_gt_f32_e64 s[40:41], v12, v3
	s_nop 1
	v_cndmask_b32_e64 v3, v3, v12, s[40:41]
	v_cndmask_b32_e64 v0, v0, 3, s[40:41]
	v_cmp_gt_f32_e64 s[40:41], v15, v3
	s_nop 1
	v_cndmask_b32_e64 v3, v3, v15, s[40:41]
	v_cndmask_b32_e64 v0, v0, 4, s[40:41]
	v_cmp_gt_f32_e64 s[40:41], v14, v3
	s_nop 1
	v_cndmask_b32_e64 v3, v3, v14, s[40:41]
	v_cmp_ngt_f32_e64 s[42:43], v2, v3
	v_cndmask_b32_e64 v0, v0, 5, s[40:41]
	s_nop 0
	v_cndmask_b32_e64 v3, v2, v3, s[42:43]
	v_cndmask_b32_e64 v0, 6, v0, s[42:43]
	v_cmp_gt_f32_e64 s[44:45], v1, v3
	s_or_b64 s[6:7], s[42:43], s[44:45]
	v_cmp_ngt_f32_e64 s[40:41], v1, v3
	v_cndmask_b32_e64 v0, v0, 7, s[44:45]
	v_cmp_eq_u32_e64 s[46:47], 0, v0
	s_or_b64 s[46:47], s[46:47], s[48:49]
	s_nop 0
	v_cndmask_b32_e64 v6, v6, v17, s[46:47]
	v_cndmask_b32_e64 v16, 0, -1, s[46:47]
	v_cmp_ne_u32_e64 s[46:47], 1, v0
	v_cmp_gt_f32_e64 s[48:49], v7, v6
	s_and_b64 s[46:47], s[46:47], s[48:49]
	v_cndmask_b32_e64 v6, v6, v7, s[46:47]
	v_cndmask_b32_e64 v16, v16, 1, s[46:47]
	v_cmp_ne_u32_e64 s[46:47], 2, v0
	v_cmp_gt_f32_e64 s[48:49], v13, v6
	s_and_b64 s[46:47], s[46:47], s[48:49]
	v_cndmask_b32_e64 v6, v6, v13, s[46:47]
	v_cndmask_b32_e64 v7, v16, 2, s[46:47]
	v_cmp_ne_u32_e64 s[46:47], 3, v0
	v_cmp_gt_f32_e64 s[48:49], v12, v6
	s_and_b64 s[46:47], s[46:47], s[48:49]
	v_cndmask_b32_e64 v6, v6, v12, s[46:47]
	v_cndmask_b32_e64 v7, v7, 3, s[46:47]
	v_cmp_ne_u32_e64 s[46:47], 4, v0
	v_cmp_gt_f32_e64 s[48:49], v15, v6
	s_and_b64 s[46:47], s[46:47], s[48:49]
	v_cndmask_b32_e64 v6, v6, v15, s[46:47]
	v_cndmask_b32_e64 v7, v7, 4, s[46:47]
	v_cmp_ne_u32_e64 s[46:47], 5, v0
	v_cmp_gt_f32_e64 s[48:49], v14, v6
	s_and_b64 s[46:47], s[46:47], s[48:49]
	v_cndmask_b32_e64 v12, v6, v14, s[46:47]
	v_cmp_gt_f32_e64 s[42:43], v2, v12
	v_cndmask_b32_e64 v7, v7, 5, s[46:47]
	s_and_b64 s[42:43], s[6:7], s[42:43]
	v_cndmask_b32_e64 v6, v7, 6, s[42:43]
	v_cndmask_b32_e64 v2, v12, v2, s[42:43]
	s_and_saveexec_b64 s[6:7], s[40:41]
	s_cbranch_execz .LBB0_794
	v_cmp_gt_f32_e64 s[40:41], v1, v2
	s_and_saveexec_b64 s[30:31], s[40:41]
	v_mov_b32_e32 v6, 7
	v_mov_b32_e32 v2, v1
	s_or_b64 exec, exec, s[30:31]
	v_mov_b32_e32 v1, v3
